# P13 hidden-activation stores marked nt as well
# baseline (speedup 1.0000x reference)
.LBB0_1390:
	s_lshl_b32 s4, s64, 8
	s_or_b32 s4, s4, s60
	v_max_f32_e32 v129, 0, v129
	v_lshl_or_b32 v162, v162, 3, s4
	v_max_f32_e32 v128, 0, v128
	v_ashrrev_i32_e32 v163, 31, v162
	v_lshlrev_b64 v[158:159], 13, v[158:159]
	v_max_f32_e32 v125, 0, v125
	v_lshl_add_u64 v[164:165], s[14:15], 0, v[158:159]
	v_lshlrev_b64 v[158:159], 1, v[162:163]
	v_max_f32_e32 v124, 0, v124
	v_lshl_add_u64 v[162:163], v[164:165], 0, v[158:159]
	v_pk_mul_f32 v[164:165], v[124:125], v[124:125]
	v_max_f32_e32 v125, 0, v131
	v_max_f32_e32 v124, 0, v130
	v_pk_mul_f32 v[130:131], v[124:125], v[124:125]
	v_max_f32_e32 v125, 0, v127
	v_max_f32_e32 v124, 0, v126
	v_max_f32_e32 v121, 0, v121
	v_max_f32_e32 v120, 0, v120
	v_pk_mul_f32 v[128:129], v[128:129], v[128:129]
	v_pk_mul_f32 v[166:167], v[124:125], v[124:125]
	v_max_f32_e32 v117, 0, v117
	v_cvt_pk_bf16_f32 v124, v128, v129
	v_cvt_pk_bf16_f32 v125, v130, v131
	v_cvt_pk_bf16_f32 v126, v164, v165
	v_cvt_pk_bf16_f32 v127, v166, v167
	v_max_f32_e32 v116, 0, v116
	global_store_dwordx4 v[162:163], v[124:127], off nt
	v_pk_mul_f32 v[120:121], v[120:121], v[120:121]
	s_andn2_b64 vcc, exec, s[38:39]
	v_pk_mul_f32 v[124:125], v[116:117], v[116:117]
	v_max_f32_e32 v117, 0, v123
	v_max_f32_e32 v116, 0, v122
	v_pk_mul_f32 v[122:123], v[116:117], v[116:117]
	v_max_f32_e32 v117, 0, v119
	v_max_f32_e32 v116, 0, v118
	v_max_f32_e32 v113, 0, v113
	v_max_f32_e32 v112, 0, v112
	v_pk_mul_f32 v[126:127], v[116:117], v[116:117]
	v_max_f32_e32 v109, 0, v109
	v_cvt_pk_bf16_f32 v116, v120, v121
	v_cvt_pk_bf16_f32 v117, v122, v123
	v_cvt_pk_bf16_f32 v118, v124, v125
	v_cvt_pk_bf16_f32 v119, v126, v127
	v_max_f32_e32 v108, 0, v108
	global_store_dwordx4 v[162:163], v[116:119], off offset:256 nt
	v_pk_mul_f32 v[112:113], v[112:113], v[112:113]
	s_mov_b64 s[4:5], -1
	v_pk_mul_f32 v[118:119], v[108:109], v[108:109]
	v_max_f32_e32 v109, 0, v115
	v_max_f32_e32 v108, 0, v114
	v_pk_mul_f32 v[114:115], v[108:109], v[108:109]
	v_max_f32_e32 v109, 0, v111
	v_max_f32_e32 v108, 0, v110
	v_max_f32_e32 v105, 0, v105
	v_lshlrev_b64 v[116:117], 13, v[156:157]
	v_max_f32_e32 v104, 0, v104
	v_lshl_add_u64 v[116:117], s[14:15], 0, v[116:117]
	v_pk_mul_f32 v[120:121], v[108:109], v[108:109]
	v_max_f32_e32 v101, 0, v101
	v_lshl_add_u64 v[116:117], v[116:117], 0, v[158:159]
	v_cvt_pk_bf16_f32 v108, v112, v113
	v_cvt_pk_bf16_f32 v109, v114, v115
	v_cvt_pk_bf16_f32 v110, v118, v119
	v_cvt_pk_bf16_f32 v111, v120, v121
	v_max_f32_e32 v100, 0, v100
	global_store_dwordx4 v[116:117], v[108:111], off nt
	v_pk_mul_f32 v[104:105], v[104:105], v[104:105]
	s_nop 0
	v_pk_mul_f32 v[108:109], v[100:101], v[100:101]
	v_max_f32_e32 v101, 0, v107
	v_max_f32_e32 v100, 0, v106
	v_pk_mul_f32 v[106:107], v[100:101], v[100:101]
	v_max_f32_e32 v101, 0, v103
	v_max_f32_e32 v100, 0, v102
	v_max_f32_e32 v97, 0, v97
	v_max_f32_e32 v96, 0, v96
	v_pk_mul_f32 v[110:111], v[100:101], v[100:101]
	v_max_f32_e32 v93, 0, v93
	v_cvt_pk_bf16_f32 v100, v104, v105
	v_cvt_pk_bf16_f32 v101, v106, v107
	v_cvt_pk_bf16_f32 v102, v108, v109
	v_cvt_pk_bf16_f32 v103, v110, v111
	v_max_f32_e32 v92, 0, v92
	global_store_dwordx4 v[116:117], v[100:103], off offset:256 nt
	v_pk_mul_f32 v[96:97], v[96:97], v[96:97]
	s_nop 0
	v_pk_mul_f32 v[102:103], v[92:93], v[92:93]
	v_max_f32_e32 v93, 0, v99
	v_max_f32_e32 v92, 0, v98
	v_pk_mul_f32 v[98:99], v[92:93], v[92:93]
	v_max_f32_e32 v93, 0, v95
	v_max_f32_e32 v92, 0, v94
	v_max_f32_e32 v89, 0, v89
	v_lshlrev_b64 v[100:101], 13, v[154:155]
	v_max_f32_e32 v88, 0, v88
	v_lshl_add_u64 v[100:101], s[14:15], 0, v[100:101]
	v_pk_mul_f32 v[104:105], v[92:93], v[92:93]
	v_max_f32_e32 v85, 0, v85
	v_lshl_add_u64 v[100:101], v[100:101], 0, v[158:159]
	v_cvt_pk_bf16_f32 v92, v96, v97
	v_cvt_pk_bf16_f32 v93, v98, v99
	v_cvt_pk_bf16_f32 v94, v102, v103
	v_cvt_pk_bf16_f32 v95, v104, v105
	v_max_f32_e32 v84, 0, v84
	global_store_dwordx4 v[100:101], v[92:95], off nt
	v_pk_mul_f32 v[88:89], v[88:89], v[88:89]
	s_nop 0
	v_pk_mul_f32 v[92:93], v[84:85], v[84:85]
	v_max_f32_e32 v85, 0, v91
	v_max_f32_e32 v84, 0, v90
	v_pk_mul_f32 v[90:91], v[84:85], v[84:85]
	v_max_f32_e32 v85, 0, v87
	v_max_f32_e32 v84, 0, v86
	v_max_f32_e32 v81, 0, v81
	v_max_f32_e32 v80, 0, v80
	v_pk_mul_f32 v[94:95], v[84:85], v[84:85]
	v_max_f32_e32 v77, 0, v77
	v_cvt_pk_bf16_f32 v84, v88, v89
	v_cvt_pk_bf16_f32 v85, v90, v91
	v_cvt_pk_bf16_f32 v86, v92, v93
	v_cvt_pk_bf16_f32 v87, v94, v95
	v_max_f32_e32 v76, 0, v76
	global_store_dwordx4 v[100:101], v[84:87], off offset:256 nt
	v_pk_mul_f32 v[80:81], v[80:81], v[80:81]
	s_nop 0
	v_pk_mul_f32 v[86:87], v[76:77], v[76:77]
	v_max_f32_e32 v77, 0, v83
	v_max_f32_e32 v76, 0, v82
	v_pk_mul_f32 v[82:83], v[76:77], v[76:77]
	v_max_f32_e32 v77, 0, v79
	v_max_f32_e32 v76, 0, v78
	v_max_f32_e32 v73, 0, v73
	v_lshlrev_b64 v[84:85], 13, v[152:153]
	v_max_f32_e32 v72, 0, v72
	v_lshl_add_u64 v[84:85], s[14:15], 0, v[84:85]
	v_pk_mul_f32 v[88:89], v[76:77], v[76:77]
	v_max_f32_e32 v69, 0, v69
	v_lshl_add_u64 v[84:85], v[84:85], 0, v[158:159]
	v_cvt_pk_bf16_f32 v76, v80, v81
	v_cvt_pk_bf16_f32 v77, v82, v83
	v_cvt_pk_bf16_f32 v78, v86, v87
	v_cvt_pk_bf16_f32 v79, v88, v89
	v_max_f32_e32 v68, 0, v68
	global_store_dwordx4 v[84:85], v[76:79], off nt
	v_pk_mul_f32 v[72:73], v[72:73], v[72:73]
	s_nop 0
	v_pk_mul_f32 v[76:77], v[68:69], v[68:69]
	v_max_f32_e32 v69, 0, v75
	v_max_f32_e32 v68, 0, v74
	v_pk_mul_f32 v[74:75], v[68:69], v[68:69]
	v_max_f32_e32 v69, 0, v71
	v_max_f32_e32 v68, 0, v70
	v_max_f32_e32 v65, 0, v65
	v_max_f32_e32 v64, 0, v64
	v_pk_mul_f32 v[78:79], v[68:69], v[68:69]
	v_max_f32_e32 v61, 0, v61
	v_cvt_pk_bf16_f32 v68, v72, v73
	v_cvt_pk_bf16_f32 v69, v74, v75
	v_cvt_pk_bf16_f32 v70, v76, v77
	v_cvt_pk_bf16_f32 v71, v78, v79
	v_max_f32_e32 v60, 0, v60
	global_store_dwordx4 v[84:85], v[68:71], off offset:256 nt
	v_pk_mul_f32 v[64:65], v[64:65], v[64:65]
	s_nop 0
	v_pk_mul_f32 v[70:71], v[60:61], v[60:61]
	v_max_f32_e32 v61, 0, v67
	v_max_f32_e32 v60, 0, v66
	v_pk_mul_f32 v[66:67], v[60:61], v[60:61]
	v_max_f32_e32 v61, 0, v63
	v_max_f32_e32 v60, 0, v62
	v_max_f32_e32 v57, 0, v57
	v_lshlrev_b64 v[68:69], 13, v[150:151]
	v_max_f32_e32 v56, 0, v56
	v_lshl_add_u64 v[68:69], s[14:15], 0, v[68:69]
	v_pk_mul_f32 v[72:73], v[60:61], v[60:61]
	v_max_f32_e32 v53, 0, v53
	v_lshl_add_u64 v[68:69], v[68:69], 0, v[158:159]
	v_cvt_pk_bf16_f32 v60, v64, v65
	v_cvt_pk_bf16_f32 v61, v66, v67
	v_cvt_pk_bf16_f32 v62, v70, v71
	v_cvt_pk_bf16_f32 v63, v72, v73
	v_max_f32_e32 v52, 0, v52
	global_store_dwordx4 v[68:69], v[60:63], off nt
	v_pk_mul_f32 v[56:57], v[56:57], v[56:57]
	s_nop 0
	v_pk_mul_f32 v[60:61], v[52:53], v[52:53]
	v_max_f32_e32 v53, 0, v59
	v_max_f32_e32 v52, 0, v58
	v_pk_mul_f32 v[58:59], v[52:53], v[52:53]
	v_max_f32_e32 v53, 0, v55
	v_max_f32_e32 v52, 0, v54
	v_max_f32_e32 v49, 0, v49
	v_max_f32_e32 v48, 0, v48
	v_pk_mul_f32 v[62:63], v[52:53], v[52:53]
	v_max_f32_e32 v45, 0, v45
	v_cvt_pk_bf16_f32 v52, v56, v57
	v_cvt_pk_bf16_f32 v53, v58, v59
	v_cvt_pk_bf16_f32 v54, v60, v61
	v_cvt_pk_bf16_f32 v55, v62, v63
	v_max_f32_e32 v44, 0, v44
	global_store_dwordx4 v[68:69], v[52:55], off offset:256 nt
	v_pk_mul_f32 v[48:49], v[48:49], v[48:49]
	s_nop 0
	v_pk_mul_f32 v[54:55], v[44:45], v[44:45]
	v_max_f32_e32 v45, 0, v51
	v_max_f32_e32 v44, 0, v50
	v_pk_mul_f32 v[50:51], v[44:45], v[44:45]
	v_max_f32_e32 v45, 0, v47
	v_max_f32_e32 v44, 0, v46
	v_max_f32_e32 v41, 0, v41
	v_lshlrev_b64 v[52:53], 13, v[148:149]
	v_max_f32_e32 v40, 0, v40
	v_lshl_add_u64 v[52:53], s[14:15], 0, v[52:53]
	v_pk_mul_f32 v[56:57], v[44:45], v[44:45]
	v_max_f32_e32 v37, 0, v37
	v_lshl_add_u64 v[52:53], v[52:53], 0, v[158:159]
	v_cvt_pk_bf16_f32 v44, v48, v49
	v_cvt_pk_bf16_f32 v45, v50, v51
	v_cvt_pk_bf16_f32 v46, v54, v55
	v_cvt_pk_bf16_f32 v47, v56, v57
	v_max_f32_e32 v36, 0, v36
	global_store_dwordx4 v[52:53], v[44:47], off nt
	v_pk_mul_f32 v[40:41], v[40:41], v[40:41]
	s_nop 0
	v_pk_mul_f32 v[44:45], v[36:37], v[36:37]
	v_max_f32_e32 v37, 0, v43
	v_max_f32_e32 v36, 0, v42
	v_pk_mul_f32 v[42:43], v[36:37], v[36:37]
	v_max_f32_e32 v37, 0, v39
	v_max_f32_e32 v36, 0, v38
	v_max_f32_e32 v33, 0, v33
	v_max_f32_e32 v32, 0, v32
	v_pk_mul_f32 v[46:47], v[36:37], v[36:37]
	v_max_f32_e32 v29, 0, v29
	v_cvt_pk_bf16_f32 v36, v40, v41
	v_cvt_pk_bf16_f32 v37, v42, v43
	v_cvt_pk_bf16_f32 v38, v44, v45
	v_cvt_pk_bf16_f32 v39, v46, v47
	v_max_f32_e32 v28, 0, v28
	global_store_dwordx4 v[52:53], v[36:39], off offset:256 nt
	v_pk_mul_f32 v[32:33], v[32:33], v[32:33]
	s_nop 0
	v_pk_mul_f32 v[38:39], v[28:29], v[28:29]
	v_max_f32_e32 v29, 0, v35
	v_max_f32_e32 v28, 0, v34
	v_pk_mul_f32 v[34:35], v[28:29], v[28:29]
	v_max_f32_e32 v29, 0, v31
	v_max_f32_e32 v28, 0, v30
	v_max_f32_e32 v25, 0, v25
	v_lshlrev_b64 v[36:37], 13, v[146:147]
	v_max_f32_e32 v24, 0, v24
	v_lshl_add_u64 v[36:37], s[14:15], 0, v[36:37]
	v_pk_mul_f32 v[40:41], v[28:29], v[28:29]
	v_max_f32_e32 v21, 0, v21
	v_lshl_add_u64 v[36:37], v[36:37], 0, v[158:159]
	v_cvt_pk_bf16_f32 v28, v32, v33
	v_cvt_pk_bf16_f32 v29, v34, v35
	v_cvt_pk_bf16_f32 v30, v38, v39
	v_cvt_pk_bf16_f32 v31, v40, v41
	v_max_f32_e32 v20, 0, v20
	global_store_dwordx4 v[36:37], v[28:31], off nt
	v_pk_mul_f32 v[24:25], v[24:25], v[24:25]
	s_nop 0
	v_pk_mul_f32 v[28:29], v[20:21], v[20:21]
	v_max_f32_e32 v21, 0, v27
	v_max_f32_e32 v20, 0, v26
	v_pk_mul_f32 v[26:27], v[20:21], v[20:21]
	v_max_f32_e32 v21, 0, v23
	v_max_f32_e32 v20, 0, v22
	v_max_f32_e32 v17, 0, v17
	v_max_f32_e32 v16, 0, v16
	v_pk_mul_f32 v[30:31], v[20:21], v[20:21]
	v_max_f32_e32 v13, 0, v13
	v_cvt_pk_bf16_f32 v20, v24, v25
	v_cvt_pk_bf16_f32 v21, v26, v27
	v_cvt_pk_bf16_f32 v22, v28, v29
	v_cvt_pk_bf16_f32 v23, v30, v31
	v_max_f32_e32 v12, 0, v12
	global_store_dwordx4 v[36:37], v[20:23], off offset:256 nt
	v_pk_mul_f32 v[16:17], v[16:17], v[16:17]
	s_nop 0
	v_pk_mul_f32 v[22:23], v[12:13], v[12:13]
	v_max_f32_e32 v13, 0, v19
	v_max_f32_e32 v12, 0, v18
	v_pk_mul_f32 v[18:19], v[12:13], v[12:13]
	v_max_f32_e32 v13, 0, v15
	v_max_f32_e32 v12, 0, v14
	v_max_f32_e32 v9, 0, v9
	v_lshlrev_b64 v[20:21], 13, v[144:145]
	v_max_f32_e32 v8, 0, v8
	v_lshl_add_u64 v[20:21], s[14:15], 0, v[20:21]
	v_pk_mul_f32 v[24:25], v[12:13], v[12:13]
	v_max_f32_e32 v5, 0, v5
	v_lshl_add_u64 v[20:21], v[20:21], 0, v[158:159]
	v_cvt_pk_bf16_f32 v12, v16, v17
	v_cvt_pk_bf16_f32 v13, v18, v19
	v_cvt_pk_bf16_f32 v14, v22, v23
	v_cvt_pk_bf16_f32 v15, v24, v25
	v_max_f32_e32 v4, 0, v4
	global_store_dwordx4 v[20:21], v[12:15], off nt
	v_pk_mul_f32 v[8:9], v[8:9], v[8:9]
	s_nop 0
	v_pk_mul_f32 v[12:13], v[4:5], v[4:5]
	v_max_f32_e32 v5, 0, v11
	v_max_f32_e32 v4, 0, v10
	v_pk_mul_f32 v[10:11], v[4:5], v[4:5]
	v_max_f32_e32 v5, 0, v7
	v_max_f32_e32 v4, 0, v6
	v_pk_mul_f32 v[14:15], v[4:5], v[4:5]
	v_cvt_pk_bf16_f32 v4, v8, v9
	v_cvt_pk_bf16_f32 v5, v10, v11
	v_cvt_pk_bf16_f32 v6, v12, v13
	v_cvt_pk_bf16_f32 v7, v14, v15
	global_store_dwordx4 v[20:21], v[4:7], off offset:256 nt
	s_cbranch_vccnz .LBB0_1372
	s_andn2_b64 vcc, exec, s[10:11]
	s_cbranch_vccnz .LBB0_1371
	s_barrier
	s_branch .LBB0_1371
